# in-proj/gates GEMM unit order: each XCD starts on a different 4-column block per round (rotated by XCD index) so the 8 XCDs do not fetch the same weight panels at the same time
# speedup vs baseline: 1.0089x; 1.0089x over previous
.LBB0_210:
	s_or_b64 exec, exec, s[0:1]
	s_waitcnt lgkmcnt(0)
	s_barrier
	s_load_dword s5, s[94:95], 0x180
	s_mov_b64 s[0:1], src_shared_base
	v_writelane_b32 v252, s0, 6
	s_mov_b32 s51, 0
	s_movk_i32 s93, 0x180
	v_writelane_b32 v252, s1, 7
	s_waitcnt lgkmcnt(0)
	s_ashr_i32 s7, s5, 3
	v_readlane_b32 s4, v252, 0
	s_ashr_i32 s6, s4, 3
	s_cmpk_lt_i32 s6, 0x120
	s_cselect_b64 s[0:1], -1, 0
	v_writelane_b32 v252, s0, 8
	s_movk_i32 s77, 0x70
	s_mov_b32 s85, 0x800000
	v_writelane_b32 v252, s1, 9
	s_lshl_b32 s0, s4, 4
	s_and_b32 s8, s0, 0x70
	s_lshr_b32 s100, s6, 5
	s_and_b32 s101, s6, 31
	s_lshr_b32 s0, s100, 2
	s_lshl_b32 s0, s0, 3
	s_and_b32 s1, s101, 7
	s_add_i32 s0, s0, s1
	s_lshr_b32 s11, s8, 4
	s_add_i32 s10, s100, s11
	s_and_b32 s10, s10, 3
	s_lshl_b32 s10, s10, 2
	s_lshr_b32 s1, s101, 3
	s_add_i32 s10, s10, s1
	s_and_b32 s1, s101, 15
	s_lshr_b32 s11, s101, 4
	s_add_i32 s11, s11, 16
	s_cmp_lt_u32 s100, 8
	s_cselect_b32 s0, s0, s1
	s_cselect_b32 s10, s10, s11
	s_add_i32 s2, s0, s8
	s_ashr_i32 s11, s10, 31
	s_lshl_b64 s[0:1], s[10:11], 19
	v_writelane_b32 v252, s0, 10
	s_waitcnt vmcnt(0)
	v_mov_b32_e32 v3, 0
	v_mov_b32_e32 v220, 0x1000
	v_writelane_b32 v252, s1, 11
	s_mov_b32 s0, s10
	v_writelane_b32 v252, s0, 12
	v_mov_b32_e32 v221, 0x2000
	v_mov_b32_e32 v219, 0x3b808081
	v_writelane_b32 v252, s1, 13
	s_add_i32 s0, s10, -12
	s_cmp_lt_u32 s0, 3
	s_cselect_b64 s[0:1], -1, 0
	v_writelane_b32 v252, s0, 14
	s_ashr_i32 s3, s2, 31
	v_mbcnt_hi_u32_b32 v214, -1, v42
	v_writelane_b32 v252, s1, 15
	s_lshl_b64 s[0:1], s[2:3], 19
	v_writelane_b32 v252, s0, 16
	v_mov_b32_e32 v226, 0x180
	v_mov_b32_e32 v232, 0x100000
	v_writelane_b32 v252, s1, 17
	s_mov_b32 s0, s2
	v_writelane_b32 v252, s0, 18
	v_mov_b32_e32 v227, 0x2080
	v_mov_b32_e32 v228, 0xff61b1e6
	v_writelane_b32 v252, s1, 19
	s_lshl_b32 s0, s2, 8
	s_cmpk_eq_i32 s5, 0x100
	v_writelane_b32 v252, s0, 20
	s_cselect_b64 s[0:1], -1, 0
	s_ashr_i32 s10, s4, 4
	v_writelane_b32 v252, s0, 21
	s_ashr_i32 s11, s10, 31
	s_and_b32 s9, s4, 15
	v_writelane_b32 v252, s1, 22
	s_lshl_b64 s[0:1], s[10:11], 2
	s_getpc_b64 s[2:3]
	s_add_u32 s2, s2, __const._Z4mega6Params.SLOT@rel32@lo+4
	s_addc_u32 s3, s3, __const._Z4mega6Params.SLOT@rel32@hi+12
	s_add_u32 s0, s2, s0
	s_addc_u32 s1, s3, s1
	v_writelane_b32 v252, s0, 23
	s_mov_b32 s2, s10
	v_mov_b32_e32 v233, 0xc8
	v_writelane_b32 v252, s1, 24
	s_lshl_b32 s0, s9, 5
	v_writelane_b32 v252, s0, 25
	s_add_i32 s0, s4, 0xffffff70
	v_writelane_b32 v252, s2, 26
	s_add_i32 s1, s10, -9
	s_cmp_lt_u32 s1, 4
	s_cselect_b32 s0, s0, 0x100000
	v_writelane_b32 v252, s3, 27
	v_writelane_b32 v252, s0, 28
	s_lshl_b32 s0, s9, 3
	s_add_i32 s1, s0, -1
	s_lshl_b32 s0, s9, 2
	v_writelane_b32 v252, s9, 29
	s_sub_i32 s0, s1, s0
	v_writelane_b32 v252, s1, 30
	s_cmpk_lt_i32 s6, 0x100
	v_writelane_b32 v252, s0, 31
	s_cselect_b64 s[0:1], -1, 0
	v_writelane_b32 v252, s0, 32
	v_mov_b32_e32 v234, 0xc0
	s_movk_i32 s91, 0xc0
	v_writelane_b32 v252, s1, 33
	s_lshr_b32 s100, s6, 5
	s_and_b32 s101, s6, 31
	s_lshr_b32 s1, s100, 2
	s_lshl_b32 s1, s1, 3
	s_and_b32 s0, s101, 7
	s_add_i32 s1, s1, s0
	s_lshr_b32 s0, s8, 4
	s_add_i32 s2, s100, s0
	s_and_b32 s2, s2, 3
	s_lshl_b32 s2, s2, 2
	s_lshr_b32 s0, s101, 3
	s_add_i32 s2, s2, s0
	v_writelane_b32 v252, s8, 34
	s_add_i32 s8, s1, s8
	s_add_i32 s3, s2, 18
	s_cmp_lt_i32 s2, 0
	s_cselect_b64 s[0:1], -1, 0
	v_writelane_b32 v252, s0, 35
	s_movk_i32 s33, 0x2400
	s_movk_i32 s96, 0xc00
	v_writelane_b32 v252, s1, 36
	s_and_b64 s[0:1], s[0:1], exec
	s_cselect_b32 s50, s3, s2
	v_writelane_b32 v252, s3, 37
	s_lshl_b64 s[0:1], s[50:51], 19
	s_add_i32 s2, s2, 6
	v_writelane_b32 v252, s0, 38
	s_cmp_lt_u32 s2, 3
	s_movk_i32 s97, 0x60
	v_writelane_b32 v252, s1, 39
	s_cselect_b64 s[0:1], -1, 0
	v_writelane_b32 v252, s0, 40
	s_ashr_i32 s9, s8, 31
	s_mov_b32 s83, 0x2aaaaaab
	v_writelane_b32 v252, s1, 41
	s_lshl_b64 s[0:1], s[8:9], 19
	v_writelane_b32 v252, s0, 42
	s_movk_i32 s86, 0xff40
	s_movk_i32 s87, 0x7fff
	v_writelane_b32 v252, s1, 43
	s_mov_b32 s0, s8
	v_writelane_b32 v252, s0, 44
	s_movk_i32 s88, 0x9ff
	s_movk_i32 s89, 0x2080
	v_writelane_b32 v252, s1, 45
	s_lshl_b32 s0, s8, 8
	s_cmpk_lt_i32 s6, 0x80
	v_writelane_b32 v252, s0, 46
	s_cselect_b64 s[0:1], -1, 0
	v_writelane_b32 v252, s0, 47
	s_mov_b32 s90, 0xff61b1e6
	s_mov_b64 s[60:61], 0x80
	v_writelane_b32 v252, s1, 48
	s_and_b32 s0, s4, 7
	s_cmp_lt_i32 s6, 64
	s_cselect_b64 s[2:3], -1, 0
	v_writelane_b32 v252, s2, 49
	s_mov_b64 s[40:41], 0x2200
	s_mov_b64 s[70:71], 0x2000
	v_writelane_b32 v252, s3, 50
	v_writelane_b32 v252, s0, 51
	s_lshl_b32 s2, s0, 4
	s_lshr_b32 s0, s6, 30
	s_add_i32 s0, s6, s0
	s_ashr_i32 s1, s0, 2
	v_writelane_b32 v252, s2, 52
	s_add_i32 s1, s2, s1
	s_and_b32 s0, s0, -4
	v_writelane_b32 v252, s1, 53
	s_sub_i32 s8, s6, s0
	s_lshl_b32 s0, s5, 3
	v_writelane_b32 v252, s0, 54
	s_mov_b64 s[80:81], 0x48000
	s_mov_b32 s82, 0x3e38aa3b
	v_writelane_b32 v252, s1, 55
	s_lshl_b32 s0, s5, 5
	v_writelane_b32 v252, s0, 56
	s_ashr_i32 s0, s4, 6
	v_writelane_b32 v252, s0, 57
	s_and_b32 s0, s6, 7
	s_cmp_lt_u32 s0, 4
	v_writelane_b32 v252, s0, 58
	s_cselect_b64 s[0:1], -1, 0
	s_abs_i32 s2, s7
	v_cvt_f32_u32_e32 v1, s2
	v_writelane_b32 v252, s0, 59
	s_mov_b32 s5, s51
	s_ashr_i32 s9, s8, 31
	v_rcp_iflag_f32_e32 v1, v1
	v_writelane_b32 v252, s1, 60
	v_writelane_b32 v252, s7, 61
	s_and_b32 s1, s6, 1
	v_mul_f32_e32 v1, 0x4f7ffffe, v1
	v_cvt_u32_f32_e32 v1, v1
	v_writelane_b32 v252, s6, 62
	s_lshl_b32 s4, s1, 7
	v_writelane_b32 v252, s4, 63
	s_lshl_b32 s1, s1, 1
	s_lshl_b32 s0, s6, 18
	v_writelane_b32 v253, s5, 0
	v_writelane_b32 v253, s1, 1
	v_writelane_b32 v253, s2, 2
	s_sub_i32 s1, 0, s2
	v_readfirstlane_b32 s2, v1
	s_mul_i32 s1, s1, s2
	s_mul_hi_u32 s1, s2, s1
	s_add_i32 s1, s2, s1
	v_writelane_b32 v253, s1, 3
	s_add_i32 s1, 0, 0x26280
	v_writelane_b32 v253, s1, 4
	s_add_i32 s1, 0, 0x26284
	v_writelane_b32 v253, s1, 5
	s_add_i32 s1, 0, 0x26288
	v_writelane_b32 v253, s1, 6
	s_add_i32 s1, 0, 0x18400
	v_writelane_b32 v253, s1, 7
	s_add_i32 s1, 0, 0x184c0
	v_writelane_b32 v253, s1, 8
	s_add_i32 s1, 0, 0x17700
	v_writelane_b32 v253, s1, 9
	s_add_i32 s1, 0, 0x17800
	v_writelane_b32 v253, s1, 10
	s_add_i32 s1, 0, 0x17100
	v_writelane_b32 v253, s1, 11
	s_add_i32 s1, 0, 0xb600
	v_writelane_b32 v253, s1, 12
	s_add_i32 s1, 0, 0x1e650
	v_writelane_b32 v253, s1, 13
	s_add_i32 s1, 0, 0x5c00
	v_writelane_b32 v253, s1, 14
	s_add_i32 s1, 0, 0x15940
	v_writelane_b32 v253, s1, 15
	s_add_i32 s1, 0, 0x15840
	v_writelane_b32 v253, s1, 16
	s_add_i32 s1, 0, 0x15f40
	v_writelane_b32 v253, s1, 17
	s_add_i32 s1, 0, 0x15240
	v_writelane_b32 v253, s1, 18
	s_add_i32 s1, 0, 0x11640
	v_writelane_b32 v253, s1, 19
	s_add_i32 s1, 0, 0x14640
	v_writelane_b32 v253, s1, 20
	s_add_i32 s1, 0, 0x14c40
	v_writelane_b32 v253, s1, 21
	s_add_i32 s1, 0, 0x15c40
	v_writelane_b32 v253, s1, 22
	s_add_i32 s1, 0, 0x15d00
	v_writelane_b32 v253, s1, 23
	s_add_i32 s1, 0, 0x15dc0
	v_writelane_b32 v253, s1, 24
	s_add_i32 s1, 0, 0x15e80
	v_writelane_b32 v253, s1, 25
	s_add_i32 s1, 0, 0x7e40
	v_writelane_b32 v253, s1, 26
	s_add_i32 s1, 0, 0x8280
	v_writelane_b32 v253, s1, 27
	s_add_i32 s1, 0, 0xa094
	v_writelane_b32 v253, s1, 28
	s_add_i32 s1, 0, 0x10380
	v_writelane_b32 v253, s1, 29
	s_add_i32 s1, 0, 0x12380
	v_writelane_b32 v253, s1, 30
	s_add_i32 s1, 0, 0x14380
	v_writelane_b32 v253, s1, 31
	s_add_i32 s1, 0, 0x16380
	v_writelane_b32 v253, s1, 32
	s_add_i32 s1, 0, 0x18380
	v_writelane_b32 v253, s1, 33
	s_add_i32 s1, 0, 0x1a380
	v_writelane_b32 v253, s1, 34
	s_add_i32 s1, 0, 0x1c380
	v_writelane_b32 v253, s1, 35
	s_add_i32 s1, 0, 0x1e380
	v_writelane_b32 v253, s1, 36
	s_add_i32 s1, 0, 0x10100
	v_writelane_b32 v253, s1, 37
	s_add_i32 s1, 0, 0x12100
	v_writelane_b32 v253, s1, 38
	s_add_i32 s1, 0, 0x16100
	v_writelane_b32 v253, s1, 39
	s_add_i32 s1, 0, 0x20060
	v_writelane_b32 v253, s1, 40
	s_add_i32 s1, 0, 0x20004
	v_writelane_b32 v253, s1, 41
	s_add_i32 s1, 0, 0x2000c
	v_writelane_b32 v253, s1, 42
	s_add_i32 s1, 0, 0x20014
	v_writelane_b32 v253, s1, 43
	s_add_i32 s1, 0, 0x2001c
	v_writelane_b32 v253, s1, 44
	s_add_i32 s1, 0, 0x20024
	v_writelane_b32 v253, s1, 45
	s_add_i32 s1, 0, 0x2002c
	v_writelane_b32 v253, s1, 46
	s_add_i32 s1, 0, 0x20034
	v_writelane_b32 v253, s1, 47
	s_add_i32 s1, 0, 0x2003c
	v_writelane_b32 v253, s1, 48
	s_add_i32 s1, 0, 0x20044
	v_writelane_b32 v253, s1, 49
	s_add_i32 s1, 0, 0x2004c
	v_writelane_b32 v253, s1, 50
	s_add_i32 s1, 0, 0x20054
	s_and_b32 s0, s0, 0xc0000
	v_writelane_b32 v253, s1, 51
	s_add_i32 s1, 0, 0x2005c
	v_writelane_b32 v253, s1, 52
	s_lshl_b32 s0, s0, 1
	v_writelane_b32 v253, s0, 53
	s_add_i32 s69, 0, 0x14100
	v_mov_b32_e32 v1, 0x358637bd
	v_writelane_b32 v253, s1, 54
	s_mov_b32 s0, 0
	v_writelane_b32 v253, s0, 55
	s_mov_b32 s0, s8
	v_writelane_b32 v253, s0, 56
	s_mov_b64 s[4:5], 0
	s_mov_b32 s84, 0x3b808081
	v_writelane_b32 v253, s1, 57
	s_lshl_b64 s[0:1], s[8:9], 19
	v_writelane_b32 v253, s0, 58
	s_nop 1
	v_writelane_b32 v253, s1, 59
	s_mov_b64 s[0:1], -1
	v_writelane_b32 v253, s0, 60
	s_nop 1
	v_writelane_b32 v253, s1, 61
	v_writelane_b32 v253, s69, 62
	v_writelane_b32 v253, s92, 63
	s_nop 1
	v_writelane_b32 v254, s93, 0
	v_writelane_b32 v254, s94, 1
	s_nop 1
	v_writelane_b32 v254, s95, 2
	s_branch .LBB0_213

.LBB0_220:
	s_add_i32 s45, s48, 1
	v_readlane_b32 s15, v252, 61
	s_mul_i32 s15, s45, s15
	v_readlane_b32 s17, v252, 62
	s_add_i32 s15, s15, s17
	s_cmpk_lt_i32 s15, 0x120
	s_cselect_b64 s[24:25], -1, 0
	s_cmpk_gt_i32 s15, 0x11f
	s_cselect_b64 s[18:19], -1, 0
	s_and_b64 vcc, exec, s[18:19]
	s_cbranch_vccnz .LBB0_222
	s_lshr_b32 s100, s15, 5
	s_and_b32 s101, s15, 31
	s_lshr_b32 s14, s100, 2
	s_lshl_b32 s14, s14, 3
	s_and_b32 vcc_lo, s101, 7
	s_add_i32 s14, s14, vcc_lo
	v_readlane_b32 vcc_hi, v252, 34
	s_lshr_b32 vcc_hi, vcc_hi, 4
	s_add_i32 s16, s100, vcc_hi
	s_and_b32 s16, s16, 3
	s_lshl_b32 s16, s16, 2
	s_lshr_b32 vcc_lo, s101, 3
	s_add_i32 s16, s16, vcc_lo
	s_and_b32 vcc_lo, s101, 15
	s_lshr_b32 vcc_hi, s101, 4
	s_add_i32 vcc_hi, vcc_hi, 16
	s_cmp_lt_u32 s100, 8
	s_cselect_b32 s14, s14, vcc_lo
	s_cselect_b32 s16, s16, vcc_hi
	v_readlane_b32 s100, v252, 34
	s_add_i32 s14, s14, s100

.LBB0_1971:
	s_add_i32 s57, s50, 1
	v_readlane_b32 s21, v252, 61
	s_mul_i32 s21, s57, s21
	v_readlane_b32 s22, v252, 62
	s_add_i32 s21, s21, s22
	s_cmpk_lt_i32 s21, 0x100
	s_cselect_b64 s[30:31], -1, 0
	s_cmpk_gt_i32 s21, 0xff
	s_cselect_b64 s[22:23], -1, 0
	s_and_b64 vcc, exec, s[22:23]
	s_cbranch_vccnz .LBB0_1973
	s_lshr_b32 s100, s21, 5
	s_and_b32 s101, s21, 31
	s_lshr_b32 s20, s100, 2
	s_lshl_b32 s20, s20, 3
	s_and_b32 s26, s101, 7
	s_add_i32 s20, s20, s26
	v_readlane_b32 s27, v252, 34
	s_lshr_b32 s27, s27, 4
	s_add_i32 s26, s100, s27
	s_and_b32 s26, s26, 3
	s_lshl_b32 s26, s26, 2
	s_lshr_b32 s21, s101, 3
	s_add_i32 s21, s21, s26
	v_readlane_b32 s27, v252, 34
	s_add_i32 s20, s20, s27
	s_add_i32 s56, s21, 18
